# speedup vs baseline: 1.0090x; 1.0090x over previous
.LBB1_1:
	s_waitcnt lgkmcnt(0)
	v_mfma_f32_32x32x16_f16 v[114:129], v[198:201], v[186:189], v[114:129]
	s_mov_b32 s44, s33
	s_mov_b32 s33, s43
	v_mfma_f32_32x32x16_f16 v[98:113], v[198:201], v[182:185], v[98:113]
	v_add_u32_e32 v219, s33, v215
	ds_read_b128 v[198:201], v219 offset:8192
	ds_read_b128 v[220:223], v219 offset:10240
	ds_read_b128 v[224:227], v219 offset:12288
	ds_read_b128 v[228:231], v219 offset:14336
	v_add_u32_e32 v219, s33, v214
	ds_read_b128 v[232:235], v219
	ds_read_b128 v[236:239], v219 offset:2048
	s_waitcnt vmcnt(10)
	v_cvt_pk_f16_f32 v162, v162, v163
	v_cvt_pk_f16_f32 v163, v164, v165
	v_cvt_pk_f16_f32 v164, v154, v155
	v_cvt_pk_f16_f32 v165, v156, v157
	v_add_u32_e32 v154, s34, v209
	ds_write_b64 v154, v[162:163]
	v_add_u32_e32 v154, s34, v248
	ds_write_b64 v154, v[164:165]
	v_mfma_f32_32x32x16_f16 v[82:97], v[194:197], v[186:189], v[82:97]
	v_add_u32_e32 v154, s34, v208
	s_waitcnt vmcnt(9)
	ds_write_b128 v154, v[158:161] offset:8192
	s_waitcnt vmcnt(8)
	ds_write_b128 v154, v[174:177] offset:16384
	v_mfma_f32_32x32x16_f16 v[66:81], v[194:197], v[182:185], v[66:81]
	v_mfma_f32_32x32x16_f16 v[50:65], v[190:193], v[186:189], v[50:65]
	s_waitcnt vmcnt(7)
	ds_write_b128 v154, v[166:169] offset:24576
	s_waitcnt vmcnt(6)
	ds_write_b128 v154, v[170:173] offset:32768
	v_mfma_f32_32x32x16_f16 v[34:49], v[190:193], v[182:185], v[34:49]
	v_add_co_u32_e64 v158, s[0:1], s36, v202
	global_load_dwordx4 v[154:157], v[252:253], off offset:-144 sc1 nt
	global_load_dwordx4 v[162:165], v[204:205], off offset:-144 sc1 nt
	v_addc_co_u32_e64 v159, s[0:1], -1, v203, s[0:1]
	v_add_co_u32_e64 v166, s[0:1], s37, v202
	v_mfma_f32_32x32x16_f16 v[18:33], v[178:181], v[186:189], v[18:33]
	s_nop 0
	v_addc_co_u32_e64 v167, s[0:1], -1, v203, s[0:1]
	global_load_dwordx4 v[158:161], v[158:159], off sc1
	s_nop 0
	global_load_dwordx4 v[174:177], v[166:167], off sc1
	v_add_co_u32_e64 v166, s[0:1], s38, v202
	s_nop 1
	v_addc_co_u32_e64 v167, s[0:1], -1, v203, s[0:1]
	v_add_co_u32_e64 v170, s[0:1], s39, v202
	v_mfma_f32_32x32x16_f16 v[2:17], v[178:181], v[182:185], v[2:17]
	s_nop 0
	v_addc_co_u32_e64 v171, s[0:1], -1, v203, s[0:1]
	global_load_dwordx4 v[166:169], v[166:167], off sc1
	s_nop 0
	global_load_dwordx4 v[170:173], v[170:171], off sc1
	v_add_u32_e32 v190, s44, v216
	ds_read_b128 v[178:181], v190 offset:8192
	ds_read_b128 v[182:185], v190 offset:10240
	ds_read_b128 v[186:189], v190 offset:12288
	ds_read_b128 v[190:193], v190 offset:14336
	v_add_u32_e32 v219, s44, v217
	ds_read_b128 v[194:197], v219
	ds_read_b128 v[240:243], v219 offset:2048
	s_waitcnt lgkmcnt(12)
	v_mfma_f32_32x32x16_f16 v[114:129], v[198:201], v[232:235], v[114:129]
	s_waitcnt lgkmcnt(11)
	v_mfma_f32_32x32x16_f16 v[98:113], v[198:201], v[236:239], v[98:113]
	v_mfma_f32_32x32x16_f16 v[82:97], v[220:223], v[232:235], v[82:97]
	v_mfma_f32_32x32x16_f16 v[66:81], v[220:223], v[236:239], v[66:81]
	v_mfma_f32_32x32x16_f16 v[50:65], v[224:227], v[232:235], v[50:65]
	v_mfma_f32_32x32x16_f16 v[34:49], v[224:227], v[236:239], v[34:49]
	v_mfma_f32_32x32x16_f16 v[18:33], v[228:231], v[232:235], v[18:33]
	v_mfma_f32_32x32x16_f16 v[2:17], v[228:231], v[236:239], v[2:17]
	s_waitcnt lgkmcnt(1)
	v_mfma_f32_32x32x16_f16 v[114:129], v[178:181], v[194:197], v[114:129]
	s_waitcnt lgkmcnt(0)
	s_barrier
	s_waitcnt lgkmcnt(0)
	v_mfma_f32_32x32x16_f16 v[98:113], v[178:181], v[240:243], v[98:113]
	v_add_u32_e32 v178, s44, v215
	ds_read_b128 v[220:223], v178 offset:8192
	ds_read_b128 v[224:227], v178 offset:10240
	ds_read_b128 v[228:231], v178 offset:12288
	ds_read_b128 v[232:235], v178 offset:14336
	v_add_u32_e32 v178, s44, v214
	ds_read_b128 v[236:239], v178
	ds_read_b128 v[244:247], v178 offset:2048
	s_waitcnt vmcnt(10)
	v_cvt_pk_f16_f32 v150, v150, v151
	v_cvt_pk_f16_f32 v151, v152, v153
	v_cvt_pk_f16_f32 v152, v142, v143
	v_cvt_pk_f16_f32 v153, v144, v145
	v_add_u32_e32 v142, s33, v209
	ds_write_b64 v142, v[150:151]
	v_add_u32_e32 v142, s33, v248
	ds_write_b64 v142, v[152:153]
	v_mfma_f32_32x32x16_f16 v[82:97], v[182:185], v[194:197], v[82:97]
	v_add_u32_e32 v142, s33, v208
	s_waitcnt vmcnt(9)
	ds_write_b128 v142, v[138:141] offset:8192
	s_waitcnt vmcnt(8)
	ds_write_b128 v142, v[146:149] offset:16384
	v_mfma_f32_32x32x16_f16 v[66:81], v[182:185], v[240:243], v[66:81]
	v_mfma_f32_32x32x16_f16 v[50:65], v[186:189], v[194:197], v[50:65]
	s_waitcnt vmcnt(7)
	ds_write_b128 v142, v[134:137] offset:24576
	s_waitcnt vmcnt(6)
	ds_write_b128 v142, v[130:133] offset:32768
	v_mfma_f32_32x32x16_f16 v[34:49], v[186:189], v[240:243], v[34:49]
	v_add_co_u32_e64 v130, s[0:1], s40, v202
	global_load_dwordx4 v[142:145], v[252:253], off offset:-16 sc1 nt
	global_load_dwordx4 v[150:153], v[204:205], off offset:-16 sc1 nt
	v_addc_co_u32_e64 v131, s[0:1], -1, v203, s[0:1]
	v_add_co_u32_e64 v132, s[0:1], s41, v202
	v_mfma_f32_32x32x16_f16 v[18:33], v[190:193], v[194:197], v[18:33]
	s_nop 0
	v_addc_co_u32_e64 v133, s[0:1], -1, v203, s[0:1]
	global_load_dwordx4 v[138:141], v[130:131], off sc1
	global_load_dwordx4 v[146:149], v[132:133], off sc1
	v_add_co_u32_e64 v130, s[0:1], s42, v202
	s_nop 1
	v_addc_co_u32_e64 v131, s[0:1], -1, v203, s[0:1]
	global_load_dwordx4 v[134:137], v[130:131], off sc1
	s_nop 0
	global_load_dwordx4 v[130:133], v[202:203], off sc1
	v_mfma_f32_32x32x16_f16 v[2:17], v[190:193], v[240:243], v[2:17]
	v_lshl_add_u64 v[202:203], v[202:203], 0, s[24:25]
	v_lshl_add_u64 v[204:205], v[204:205], 0, s[26:27]
	v_lshl_add_u64 v[252:253], v[252:253], 0, s[26:27]
	v_add_u32_e32 v178, s34, v216
	ds_read_b128 v[198:201], v178 offset:8192
	ds_read_b128 v[194:197], v178 offset:10240
	ds_read_b128 v[190:193], v178 offset:12288
	ds_read_b128 v[178:181], v178 offset:14336
	v_add_u32_e32 v182, s34, v217
	ds_read_b128 v[186:189], v182
	ds_read_b128 v[182:185], v182 offset:2048
	s_waitcnt lgkmcnt(12)
	v_mfma_f32_32x32x16_f16 v[114:129], v[220:223], v[236:239], v[114:129]
	s_waitcnt lgkmcnt(11)
	v_mfma_f32_32x32x16_f16 v[98:113], v[220:223], v[244:247], v[98:113]
	v_mfma_f32_32x32x16_f16 v[82:97], v[224:227], v[236:239], v[82:97]
	v_mfma_f32_32x32x16_f16 v[66:81], v[224:227], v[244:247], v[66:81]
	v_mfma_f32_32x32x16_f16 v[50:65], v[228:231], v[236:239], v[50:65]
	v_mfma_f32_32x32x16_f16 v[34:49], v[228:231], v[244:247], v[34:49]
	v_mfma_f32_32x32x16_f16 v[18:33], v[232:235], v[236:239], v[18:33]
	v_mfma_f32_32x32x16_f16 v[2:17], v[232:235], v[244:247], v[2:17]
	s_waitcnt lgkmcnt(0)
	s_barrier
	s_add_i32 s35, s35, 2
	s_mov_b32 s43, s34
	s_cmp_gt_u32 s35, 9
	s_mov_b32 s34, s44
	s_cbranch_scc0 .LBB1_1
	s_and_b64 s[0:1], s[20:21], exec
	s_cselect_b32 s6, s6, s8
	s_cselect_b32 s7, s7, s9
	s_and_b64 s[0:1], vcc, exec
	s_cselect_b32 s1, s5, s7
	s_cselect_b32 s0, s4, s6
	v_mov_b32_e32 v202, 0x3e38aa3b
	s_waitcnt lgkmcnt(1)
	v_mfma_f32_32x32x16_f16 v[114:129], v[198:201], v[186:189], v[114:129]
	v_cndmask_b32_e32 v202, 1.0, v202, vcc
	s_waitcnt lgkmcnt(0)
	v_mfma_f32_32x32x16_f16 v[98:113], v[198:201], v[182:185], v[98:113]
	ds_read_b128 v[198:201], v215 offset:8192
	ds_read_b128 v[220:223], v215 offset:10240
	ds_read_b128 v[224:227], v215 offset:12288
	ds_read_b128 v[228:231], v215 offset:14336
	ds_read_b128 v[232:235], v214
	ds_read_b128 v[236:239], v214 offset:2048
	s_waitcnt vmcnt(10)
	v_cvt_pk_f16_f32 v162, v162, v163
	v_cvt_pk_f16_f32 v163, v164, v165
	v_cvt_pk_f16_f32 v164, v154, v155
	v_cvt_pk_f16_f32 v165, v156, v157
	v_add_u32_e32 v154, 0x14000, v209
	ds_write_b64 v154, v[162:163]
	v_add_u32_e32 v154, 0x14000, v248
	ds_write_b64 v154, v[164:165]
	v_add_u32_e32 v154, 0x14000, v213
	s_waitcnt vmcnt(9)
	ds_write_b128 v154, v[158:161]
	v_add_u32_e32 v154, 0x16000, v213
	v_mfma_f32_32x32x16_f16 v[82:97], v[194:197], v[186:189], v[82:97]
	s_waitcnt vmcnt(8)
	ds_write_b128 v154, v[174:177]
	v_mfma_f32_32x32x16_f16 v[66:81], v[194:197], v[182:185], v[66:81]
	v_add_u32_e32 v154, 0x18000, v213
	s_waitcnt vmcnt(7)
	ds_write_b128 v154, v[166:169]
	v_add_u32_e32 v154, 0x1a000, v213
	v_mfma_f32_32x32x16_f16 v[50:65], v[190:193], v[186:189], v[50:65]
	s_waitcnt vmcnt(6)
	ds_write_b128 v154, v[170:173]
	v_mfma_f32_32x32x16_f16 v[34:49], v[190:193], v[182:185], v[34:49]
	v_mfma_f32_32x32x16_f16 v[18:33], v[178:181], v[186:189], v[18:33]
	v_mfma_f32_32x32x16_f16 v[2:17], v[178:181], v[182:185], v[2:17]
	ds_read_b128 v[154:157], v216 offset:49152
	ds_read_b128 v[158:161], v216 offset:51200
	ds_read_b128 v[162:165], v216 offset:53248
	ds_read_b128 v[166:169], v216 offset:55296
	ds_read_b128 v[170:173], v217 offset:40960
	ds_read_b128 v[174:177], v217 offset:43008
	s_waitcnt lgkmcnt(12)
	v_mfma_f32_32x32x16_f16 v[114:129], v[198:201], v[232:235], v[114:129]
	s_waitcnt lgkmcnt(11)
	v_mfma_f32_32x32x16_f16 v[98:113], v[198:201], v[236:239], v[98:113]
	v_mfma_f32_32x32x16_f16 v[82:97], v[220:223], v[232:235], v[82:97]
	v_mfma_f32_32x32x16_f16 v[66:81], v[220:223], v[236:239], v[66:81]
	v_mfma_f32_32x32x16_f16 v[50:65], v[224:227], v[232:235], v[50:65]
	v_mfma_f32_32x32x16_f16 v[34:49], v[224:227], v[236:239], v[34:49]
	v_mfma_f32_32x32x16_f16 v[18:33], v[228:231], v[232:235], v[18:33]
	v_mfma_f32_32x32x16_f16 v[2:17], v[228:231], v[236:239], v[2:17]
	s_waitcnt lgkmcnt(0)
	s_barrier
	s_waitcnt lgkmcnt(1)
	v_mfma_f32_32x32x16_f16 v[114:129], v[154:157], v[170:173], v[114:129]
	s_waitcnt lgkmcnt(0)
	v_mfma_f32_32x32x16_f16 v[98:113], v[154:157], v[174:177], v[98:113]
	ds_read_b128 v[154:157], v215 offset:49152
	ds_read_b128 v[178:181], v215 offset:51200
	ds_read_b128 v[182:185], v215 offset:53248
	ds_read_b128 v[186:189], v215 offset:55296
	ds_read_b128 v[190:193], v214 offset:40960
	ds_read_b128 v[194:197], v214 offset:43008
	s_waitcnt vmcnt(4)
	v_cvt_pk_f16_f32 v150, v150, v151
	v_cvt_pk_f16_f32 v151, v152, v153
	v_cvt_pk_f16_f32 v152, v142, v143
	v_cvt_pk_f16_f32 v153, v144, v145
	ds_write_b64 v209, v[150:151]
	ds_write_b64 v248, v[152:153]
	v_mfma_f32_32x32x16_f16 v[82:97], v[158:161], v[170:173], v[82:97]
	s_waitcnt vmcnt(3)
	ds_write_b128 v208, v[138:141] offset:8192
	s_waitcnt vmcnt(2)
	ds_write_b128 v208, v[146:149] offset:16384
	v_mfma_f32_32x32x16_f16 v[66:81], v[158:161], v[174:177], v[66:81]
	v_mfma_f32_32x32x16_f16 v[50:65], v[162:165], v[170:173], v[50:65]
	s_waitcnt vmcnt(1)
	ds_write_b128 v208, v[134:137] offset:24576
	s_waitcnt vmcnt(0)
	ds_write_b128 v208, v[130:133] offset:32768
	v_mfma_f32_32x32x16_f16 v[34:49], v[162:165], v[174:177], v[34:49]
	v_mfma_f32_32x32x16_f16 v[18:33], v[166:169], v[170:173], v[18:33]
	v_mfma_f32_32x32x16_f16 v[2:17], v[166:169], v[174:177], v[2:17]
	v_add_u32_e32 v158, 0x16000, v211
	v_add_u32_e32 v142, v158, v210
	ds_read_b128 v[130:133], v142
	ds_read_b128 v[134:137], v142 offset:2048
	ds_read_b128 v[138:141], v142 offset:4096
	ds_read_b128 v[142:145], v142 offset:6144
	v_add_u32_e32 v166, 0x14000, v218
	v_add_u32_e32 v150, v166, v210
	ds_read_b128 v[146:149], v150
	ds_read_b128 v[150:153], v150 offset:2048
	s_waitcnt lgkmcnt(12)
	v_mfma_f32_32x32x16_f16 v[114:129], v[154:157], v[190:193], v[114:129]
	s_waitcnt lgkmcnt(11)
	v_mfma_f32_32x32x16_f16 v[98:113], v[154:157], v[194:197], v[98:113]
	v_mfma_f32_32x32x16_f16 v[82:97], v[178:181], v[190:193], v[82:97]
	v_mfma_f32_32x32x16_f16 v[66:81], v[178:181], v[194:197], v[66:81]
	v_mfma_f32_32x32x16_f16 v[50:65], v[182:185], v[190:193], v[50:65]
	v_mfma_f32_32x32x16_f16 v[34:49], v[182:185], v[194:197], v[34:49]
	v_mfma_f32_32x32x16_f16 v[18:33], v[186:189], v[190:193], v[18:33]
	v_mfma_f32_32x32x16_f16 v[2:17], v[186:189], v[194:197], v[2:17]
	s_waitcnt lgkmcnt(0)
	s_barrier
	s_waitcnt lgkmcnt(1)
	v_mfma_f32_32x32x16_f16 v[114:129], v[130:133], v[146:149], v[114:129]
	s_waitcnt lgkmcnt(0)
	v_mfma_f32_32x32x16_f16 v[98:113], v[130:133], v[150:153], v[98:113]
	v_add_u32_e32 v162, v158, v212
	ds_read_b128 v[130:133], v162
	ds_read_b128 v[154:157], v162 offset:2048
	ds_read_b128 v[158:161], v162 offset:4096
	ds_read_b128 v[162:165], v162 offset:6144
	v_add_u32_e32 v170, v166, v212
	ds_read_b128 v[166:169], v170
	ds_read_b128 v[170:173], v170 offset:2048
	v_mfma_f32_32x32x16_f16 v[82:97], v[134:137], v[146:149], v[82:97]
	v_mfma_f32_32x32x16_f16 v[66:81], v[134:137], v[150:153], v[66:81]
	v_mfma_f32_32x32x16_f16 v[50:65], v[138:141], v[146:149], v[50:65]
	v_mfma_f32_32x32x16_f16 v[34:49], v[138:141], v[150:153], v[34:49]
	v_mfma_f32_32x32x16_f16 v[18:33], v[142:145], v[146:149], v[18:33]
	v_mfma_f32_32x32x16_f16 v[2:17], v[142:145], v[150:153], v[2:17]
	ds_read_b128 v[134:137], v216 offset:8192
	ds_read_b128 v[138:141], v216 offset:10240
	ds_read_b128 v[142:145], v216 offset:12288
	ds_read_b128 v[146:149], v216 offset:14336
	ds_read_b128 v[150:153], v217
	ds_read_b128 v[174:177], v217 offset:2048
	s_waitcnt lgkmcnt(7)
	v_mfma_f32_32x32x16_f16 v[114:129], v[130:133], v[166:169], v[114:129]
	s_waitcnt lgkmcnt(6)
	v_mfma_f32_32x32x16_f16 v[98:113], v[130:133], v[170:173], v[98:113]
	v_mfma_f32_32x32x16_f16 v[82:97], v[154:157], v[166:169], v[82:97]
	v_mfma_f32_32x32x16_f16 v[66:81], v[154:157], v[170:173], v[66:81]
	v_mfma_f32_32x32x16_f16 v[50:65], v[158:161], v[166:169], v[50:65]
	v_mfma_f32_32x32x16_f16 v[34:49], v[158:161], v[170:173], v[34:49]
	v_mfma_f32_32x32x16_f16 v[18:33], v[162:165], v[166:169], v[18:33]
	v_mfma_f32_32x32x16_f16 v[2:17], v[162:165], v[170:173], v[2:17]
	s_waitcnt lgkmcnt(0)
	s_barrier
	s_waitcnt lgkmcnt(1)
	v_mfma_f32_32x32x16_f16 v[114:129], v[134:137], v[150:153], v[114:129]
	s_waitcnt lgkmcnt(0)
	v_mfma_f32_32x32x16_f16 v[98:113], v[134:137], v[174:177], v[98:113]
	ds_read_b128 v[130:133], v215 offset:8192
	ds_read_b128 v[134:137], v215 offset:10240
	ds_read_b128 v[154:157], v215 offset:12288
	ds_read_b128 v[158:161], v215 offset:14336
	ds_read_b128 v[162:165], v214
	ds_read_b128 v[166:169], v214 offset:2048
	v_mfma_f32_32x32x16_f16 v[82:97], v[138:141], v[150:153], v[82:97]
	v_mfma_f32_32x32x16_f16 v[66:81], v[138:141], v[174:177], v[66:81]
	v_mfma_f32_32x32x16_f16 v[50:65], v[142:145], v[150:153], v[50:65]
	v_mfma_f32_32x32x16_f16 v[34:49], v[142:145], v[174:177], v[34:49]
	v_mfma_f32_32x32x16_f16 v[18:33], v[146:149], v[150:153], v[18:33]
	v_mfma_f32_32x32x16_f16 v[2:17], v[146:149], v[174:177], v[2:17]
	s_waitcnt lgkmcnt(1)
	v_mfma_f32_32x32x16_f16 v[114:129], v[130:133], v[162:165], v[114:129]
	s_waitcnt lgkmcnt(0)
	v_mfma_f32_32x32x16_f16 v[98:113], v[130:133], v[166:169], v[98:113]
	v_mfma_f32_32x32x16_f16 v[82:97], v[134:137], v[162:165], v[82:97]
	v_mfma_f32_32x32x16_f16 v[66:81], v[134:137], v[166:169], v[66:81]
	v_mfma_f32_32x32x16_f16 v[50:65], v[154:157], v[162:165], v[50:65]
	v_mfma_f32_32x32x16_f16 v[34:49], v[154:157], v[166:169], v[34:49]
	v_mfma_f32_32x32x16_f16 v[18:33], v[158:161], v[162:165], v[18:33]
	v_mfma_f32_32x32x16_f16 v[2:17], v[158:161], v[166:169], v[2:17]
	v_lshl_or_b32 v130, v207, 2, s31
	s_waitcnt lgkmcnt(0)
	s_barrier
	s_cbranch_vccnz .Lepi_q
	v_lshlrev_b32_e32 v154, 2, v130
	global_load_dwordx4 v[134:137], v154, s[0:1]
	global_load_dwordx4 v[150:153], v154, s[0:1] offset:32
	global_load_dwordx4 v[156:159], v154, s[0:1] offset:64
	global_load_dwordx4 v[160:163], v154, s[0:1] offset:96
	global_load_dwordx4 v[164:167], v154, s[0:1] offset:128
	global_load_dwordx4 v[168:171], v154, s[0:1] offset:160
	s_movk_i32 s4, 0x410
	v_lshlrev_b32_e32 v130, 1, v130
	v_mul_lo_u32 v131, v206, s4
	v_add3_u32 v155, 0, v130, v131
	global_load_dwordx4 v[172:175], v154, s[0:1] offset:192
	global_load_dwordx4 v[146:149], v154, s[0:1] offset:224
	global_load_dwordx4 v[142:145], v154, s[0:1] offset:256
	global_load_dwordx4 v[130:133], v154, s[0:1] offset:288
	global_load_dwordx4 v[138:141], v154, s[0:1] offset:320
	v_add_u32_e32 v176, 0x8000, v155
	s_waitcnt vmcnt(10)
	v_pk_add_f32 v[114:115], v[134:135], v[114:115]
	v_pk_add_f32 v[116:117], v[136:137], v[116:117]
	v_pk_add_f32 v[98:99], v[134:135], v[98:99]
	v_pk_add_f32 v[100:101], v[136:137], v[100:101]
	s_waitcnt vmcnt(9)
	v_pk_add_f32 v[118:119], v[150:151], v[118:119]
	v_pk_add_f32 v[120:121], v[152:153], v[120:121]
	s_waitcnt vmcnt(6)
	v_pk_add_f32 v[82:83], v[164:165], v[82:83]
	v_pk_add_f32 v[84:85], v[166:167], v[84:85]
	v_pk_add_f32 v[66:67], v[164:165], v[66:67]
	v_pk_add_f32 v[68:69], v[166:167], v[68:69]
	s_waitcnt vmcnt(5)
	v_pk_add_f32 v[70:71], v[168:169], v[70:71]
	v_pk_add_f32 v[72:73], v[170:171], v[72:73]
	v_pk_add_f32 v[102:103], v[150:151], v[102:103]
	v_pk_add_f32 v[104:105], v[152:153], v[104:105]
	v_pk_add_f32 v[122:123], v[156:157], v[122:123]
	v_pk_add_f32 v[124:125], v[158:159], v[124:125]
	v_pk_add_f32 v[106:107], v[156:157], v[106:107]
	v_pk_add_f32 v[108:109], v[158:159], v[108:109]
	v_pk_add_f32 v[126:127], v[160:161], v[126:127]
	v_pk_add_f32 v[128:129], v[162:163], v[128:129]
	v_pk_add_f32 v[110:111], v[160:161], v[110:111]
	v_pk_add_f32 v[112:113], v[162:163], v[112:113]
	v_pk_add_f32 v[86:87], v[168:169], v[86:87]
	v_pk_add_f32 v[88:89], v[170:171], v[88:89]
	v_cvt_pk_f16_f32 v114, v114, v115
	v_cvt_pk_f16_f32 v115, v116, v117
	v_cvt_pk_f16_f32 v98, v98, v99
	v_cvt_pk_f16_f32 v99, v100, v101
	v_cvt_pk_f16_f32 v100, v118, v119
	v_cvt_pk_f16_f32 v101, v120, v121
	v_cvt_pk_f16_f32 v82, v82, v83
	v_cvt_pk_f16_f32 v83, v84, v85
	v_cvt_pk_f16_f32 v84, v66, v67
	v_cvt_pk_f16_f32 v85, v68, v69
	v_cvt_pk_f16_f32 v70, v70, v71
	v_cvt_pk_f16_f32 v71, v72, v73
	v_cvt_pk_f16_f32 v102, v102, v103
	v_cvt_pk_f16_f32 v103, v104, v105
	v_cvt_pk_f16_f32 v104, v122, v123
	v_cvt_pk_f16_f32 v105, v124, v125
	v_cvt_pk_f16_f32 v106, v106, v107
	v_cvt_pk_f16_f32 v107, v108, v109
	v_cvt_pk_f16_f32 v108, v126, v127
	v_cvt_pk_f16_f32 v109, v128, v129
	v_cvt_pk_f16_f32 v110, v110, v111
	v_cvt_pk_f16_f32 v111, v112, v113
	v_cvt_pk_f16_f32 v86, v86, v87
	ds_write2_b64 v155, v[114:115], v[100:101] offset1:2
	ds_write2_b64 v176, v[98:99], v[102:103] offset0:64 offset1:66
	ds_write2_b64 v155, v[104:105], v[108:109] offset0:4 offset1:6
	ds_write2_b64 v176, v[106:107], v[110:111] offset0:68 offset1:70
	v_cvt_pk_f16_f32 v87, v88, v89
	ds_write2_b64 v176, v[84:85], v[70:71] offset0:72 offset1:74
	s_waitcnt vmcnt(4)
	v_pk_add_f32 v[70:71], v[172:173], v[90:91]
	v_pk_add_f32 v[84:85], v[174:175], v[92:93]
	v_pk_add_f32 v[74:75], v[172:173], v[74:75]
	ds_write2_b64 v155, v[82:83], v[86:87] offset0:8 offset1:10
	v_mov_b64_e32 v[82:83], v[70:71]
	global_load_dwordx4 v[66:69], v154, s[0:1] offset:352
	global_load_dwordx4 v[70:73], v154, s[0:1] offset:384
	v_cvt_pk_f16_f32 v82, v82, v83
	v_cvt_pk_f16_f32 v83, v84, v85
	v_cvt_pk_f16_f32 v84, v74, v75
	v_pk_add_f32 v[74:75], v[174:175], v[76:77]
	s_waitcnt vmcnt(5)
	v_pk_add_f32 v[78:79], v[146:147], v[78:79]
	v_cvt_pk_f16_f32 v85, v74, v75
	global_load_dwordx4 v[74:77], v154, s[0:1] offset:416
	v_pk_add_f32 v[80:81], v[148:149], v[80:81]
	v_cvt_pk_f16_f32 v78, v78, v79
	v_cvt_pk_f16_f32 v79, v80, v81
	ds_write2_b64 v176, v[84:85], v[78:79] offset0:76 offset1:78
	global_load_dwordx4 v[78:81], v154, s[0:1] offset:448
	v_pk_add_f32 v[86:87], v[146:147], v[94:95]
	v_pk_add_f32 v[88:89], v[148:149], v[96:97]
	s_waitcnt vmcnt(6)
	v_pk_add_f32 v[50:51], v[142:143], v[50:51]
	v_pk_add_f32 v[52:53], v[144:145], v[52:53]
	v_pk_add_f32 v[34:35], v[142:143], v[34:35]
	v_cvt_pk_f16_f32 v86, v86, v87
	v_cvt_pk_f16_f32 v87, v88, v89
	v_cvt_pk_f16_f32 v50, v50, v51
	v_cvt_pk_f16_f32 v51, v52, v53
	v_cvt_pk_f16_f32 v52, v34, v35
	v_pk_add_f32 v[34:35], v[144:145], v[36:37]
	ds_write2_b64 v155, v[82:83], v[86:87] offset0:12 offset1:14
	v_mov_b64_e32 v[82:83], v[34:35]
	global_load_dwordx4 v[34:37], v154, s[0:1] offset:480
	s_waitcnt vmcnt(6)
	v_pk_add_f32 v[38:39], v[130:131], v[38:39]
	v_pk_add_f32 v[40:41], v[132:133], v[40:41]
	v_cvt_pk_f16_f32 v53, v82, v83
	v_cvt_pk_f16_f32 v38, v38, v39
	v_cvt_pk_f16_f32 v39, v40, v41
	ds_write2_b64 v176, v[52:53], v[38:39] offset0:80 offset1:82
	s_waitcnt vmcnt(5)
	v_pk_add_f32 v[38:39], v[138:139], v[58:59]
	v_pk_add_f32 v[40:41], v[140:141], v[60:61]
	v_cvt_pk_f16_f32 v38, v38, v39
	v_cvt_pk_f16_f32 v39, v40, v41
	v_pk_add_f32 v[40:41], v[138:139], v[42:43]
	v_pk_add_f32 v[42:43], v[140:141], v[44:45]
	v_cvt_pk_f16_f32 v40, v40, v41
	v_cvt_pk_f16_f32 v41, v42, v43
	v_pk_add_f32 v[54:55], v[130:131], v[54:55]
	v_pk_add_f32 v[56:57], v[132:133], v[56:57]
	v_cmp_gt_u32_e64 s[0:1], 8, v0
	v_cvt_pk_f16_f32 v54, v54, v55
	v_cvt_pk_f16_f32 v55, v56, v57
	s_and_b64 s[6:7], s[20:21], s[0:1]
	ds_write2_b64 v155, v[50:51], v[54:55] offset0:16 offset1:18
	s_waitcnt vmcnt(4)
	v_pk_add_f32 v[42:43], v[66:67], v[62:63]
	s_waitcnt vmcnt(3)
	v_pk_add_f32 v[18:19], v[70:71], v[18:19]
	v_pk_add_f32 v[20:21], v[72:73], v[20:21]
	v_pk_add_f32 v[2:3], v[70:71], v[2:3]
	v_pk_add_f32 v[4:5], v[72:73], v[4:5]
	v_cvt_pk_f16_f32 v18, v18, v19
	v_cvt_pk_f16_f32 v19, v20, v21
	v_cvt_pk_f16_f32 v2, v2, v3
	v_cvt_pk_f16_f32 v3, v4, v5
	s_waitcnt vmcnt(2)
	v_pk_add_f32 v[4:5], v[74:75], v[22:23]
	v_pk_add_f32 v[20:21], v[76:77], v[24:25]
	v_cvt_pk_f16_f32 v4, v4, v5
	v_cvt_pk_f16_f32 v5, v20, v21
	ds_write2_b64 v155, v[18:19], v[4:5] offset0:24 offset1:26
	v_pk_add_f32 v[4:5], v[74:75], v[6:7]
	v_pk_add_f32 v[6:7], v[76:77], v[8:9]
	v_cvt_pk_f16_f32 v4, v4, v5
	v_cvt_pk_f16_f32 v5, v6, v7
	ds_write2_b64 v176, v[2:3], v[4:5] offset0:88 offset1:90
	s_waitcnt vmcnt(1)
	v_pk_add_f32 v[2:3], v[78:79], v[26:27]
	v_pk_add_f32 v[4:5], v[80:81], v[28:29]
	v_cvt_pk_f16_f32 v2, v2, v3
	v_cvt_pk_f16_f32 v3, v4, v5
	v_pk_add_f32 v[4:5], v[78:79], v[10:11]
	v_pk_add_f32 v[6:7], v[80:81], v[12:13]
	v_pk_add_f32 v[44:45], v[68:69], v[64:65]
	v_cvt_pk_f16_f32 v4, v4, v5
	v_cvt_pk_f16_f32 v5, v6, v7
	s_waitcnt vmcnt(0)
	v_pk_add_f32 v[6:7], v[34:35], v[30:31]
	v_pk_add_f32 v[8:9], v[36:37], v[32:33]
	v_cvt_pk_f16_f32 v42, v42, v43
	v_cvt_pk_f16_f32 v43, v44, v45
	v_cvt_pk_f16_f32 v6, v6, v7
	v_cvt_pk_f16_f32 v7, v8, v9
	ds_write2_b64 v155, v[38:39], v[42:43] offset0:20 offset1:22
	v_pk_add_f32 v[38:39], v[66:67], v[46:47]
	v_pk_add_f32 v[42:43], v[68:69], v[48:49]
	ds_write2_b64 v155, v[2:3], v[6:7] offset0:28 offset1:30
	v_pk_add_f32 v[2:3], v[34:35], v[14:15]
	v_pk_add_f32 v[6:7], v[36:37], v[16:17]
	v_cvt_pk_f16_f32 v38, v38, v39
	v_cvt_pk_f16_f32 v39, v42, v43
	v_cvt_pk_f16_f32 v2, v2, v3
	v_cvt_pk_f16_f32 v3, v6, v7
	ds_write2_b64 v176, v[40:41], v[38:39] offset0:84 offset1:86
	ds_write2_b64 v176, v[4:5], v[2:3] offset0:92 offset1:94
	s_branch .Lepi_join
